# baseline (speedup 1.0000x reference)
.LBB0_95:
	s_lshl_b32 s94, s97, 4
	v_add_u32_e32 v2, s94, v79
	v_cmp_gt_i32_e32 vcc, s100, v2
	v_add_u32_e32 v2, s98, v2
	s_mov_b64 s[30:31], vcc
	v_cndmask_b32_e32 v2, 0, v2, vcc
	v_lshlrev_b32_e32 v108, 2, v2
	v_cmp_lt_i32_e32 vcc, -1, v55
	v_lshl_add_u32 v87, v55, 8, v70
	s_mov_b64 s[90:91], vcc
	v_cndmask_b32_e32 v87, v70, v87, vcc
	s_cmp_lt_i32 s86, s68
	s_cselect_b64 s[78:79], -1, 0
	s_lshl_b32 s94, s81, 4
	s_add_i32 s95, s94, 16
	s_cmp_ge_i32 s95, s83
	s_cselect_b64 s[0:1], -1, 0
	s_and_b64 s[42:43], s[78:79], s[0:1]
	s_waitcnt vmcnt(0)
	s_and_saveexec_b64 s[40:41], s[42:43]
	s_cbranch_execz .LBB0_97
	s_lshl_b32 s95, s86, 1
	v_mov_b32_e32 v99, s95
	v_or_b32_e32 v100, 1, v99
	v_min_i32_e32 v100, s67, v100
	v_cndmask_b32_e64 v99, v100, v99, s[38:39]
	v_add_u32_e32 v100, s66, v99
	v_ashrrev_i32_e32 v101, 31, v100
	v_lshlrev_b64 v[100:101], 8, v[100:101]
	v_lshl_add_u64 v[100:101], v[72:73], 0, v[100:101]
	global_load_dwordx4 v[112:115], v[100:101], off nt
.LBB0_97:
	s_or_b64 exec, exec, s[40:41]
	global_load_dword v98, v108, s[58:59]
	s_cmp_lt_i32 s80, 0
	s_cbranch_scc1 .Lattn_k0
	v_mfma_f32_16x16x32_f16 v[104:107], v[74:77], v[6:9], 0
	v_or_b32_e32 v2, s94, v79
	v_cmp_lt_i32_e64 s[42:43], v2, s82
	v_cmp_ge_i32_e64 s[40:41], v2, s82
	v_mfma_f32_16x16x32_f16 v[104:107], v[94:97], v[10:13], v[104:107]
	s_and_b64 s[42:43], s[84:85], s[42:43]
	v_cndmask_b32_e64 v2, 0, 1, s[42:43]
	s_and_b64 s[40:41], s[40:41], s[84:85]
	v_cmp_ne_u32_e64 s[42:43], 0, v2
	v_cndmask_b32_e64 v2, 0, 1, s[40:41]
	v_mfma_f32_16x16x32_f16 v[104:107], v[120:123], v[14:17], v[104:107]
	v_cmp_ne_u32_e32 vcc, 0, v2
	v_mov_b32_e32 v5, s42
	v_cmp_ngt_f32_e64 s[48:49], s70, v103
	v_mov_b32_e32 v2, vcc_lo
	v_cndmask_b32_e64 v2, v2, v5, s[38:39]
	v_mfma_f32_16x16x32_f16 v[108:111], v[124:127], v[18:21], v[104:107]
	ds_write2_b64 v92, v[74:75], v[76:77] offset1:4
	ds_write2_b64 v92, v[94:95], v[96:97] offset0:8 offset1:12
	ds_read_b64_tr_b16 v[62:63], v93
	ds_read_b64_tr_b16 v[64:65], v93 offset:32
	ds_read_b64_tr_b16 v[68:69], v93 offset:64
	ds_read_b64_tr_b16 v[84:85], v93 offset:96
	ds_write2_b64 v92, v[120:121], v[122:123] offset1:4
	ds_write2_b64 v92, v[124:125], v[126:127] offset0:8 offset1:12
	ds_read_b64_tr_b16 v[54:55], v93
	ds_read_b64_tr_b16 v[56:57], v93 offset:32
	ds_read_b64_tr_b16 v[58:59], v93 offset:64
	ds_read_b64_tr_b16 v[60:61], v93 offset:96
	global_load_dwordx4 v[74:77], v87, s[92:93]
	global_load_dwordx4 v[94:97], v87, s[92:93] offset:64
	global_load_dwordx4 v[120:123], v87, s[92:93] offset:128
	global_load_dwordx4 v[124:127], v87, s[92:93] offset:192
	v_lshrrev_b32_sdwa v2, v88, v2 dst_sel:DWORD dst_unused:UNUSED_PAD src0_sel:DWORD src1_sel:WORD_0
	v_and_b32_e32 v5, 1, v2
	v_cmp_eq_u32_e64 s[46:47], 0, v5
	v_and_b32_e32 v5, 2, v2
	v_cmp_eq_u32_e64 s[40:41], 0, v5
	v_and_b32_e32 v104, 4, v2
	v_and_b32_e32 v2, 8, v2
	s_nop 0
	v_cndmask_b32_e64 v107, v108, v71, s[46:47]
	v_cndmask_b32_e64 v105, v109, v71, s[40:41]
	v_cmp_eq_u32_e64 s[42:43], 0, v104
	v_cmp_eq_u32_e64 s[44:45], 0, v2
	v_max3_f32 v5, v107, s69, v105
	v_cndmask_b32_e64 v106, v110, v71, s[42:43]
	v_cndmask_b32_e64 v104, v111, v71, s[44:45]
	v_max3_f32 v2, v5, v106, v104
	v_mov_b32_e32 v5, v2
	s_nop 1
	v_permlane16_swap_b32_e32 v5, v2
	v_max_f32_e32 v2, v2, v5
	v_mov_b32_e32 v5, v2
	s_nop 1
	v_permlane32_swap_b32_e32 v5, v2
	v_max_f32_e32 v108, v2, v5
	v_sub_f32_e32 v2, v108, v103
	v_cmp_lt_f32_e32 vcc, s71, v2
	s_and_b64 vcc, s[48:49], vcc
	s_nop 0
	v_cndmask_b32_e64 v2, 0, 1, vcc
	v_cmp_ne_u32_e64 s[50:51], 0, v2
	s_cmp_lg_u64 s[50:51], 0
	s_cselect_b64 s[50:51], -1, 0
	s_cbranch_vccz .LBB0_117
	v_max_f32_e32 v2, v108, v108
	v_max_f32_e32 v5, v103, v103
	v_max_f32_e32 v5, v5, v2
	v_sub_f32_e32 v2, v103, v5
	v_exp_f32_e32 v2, v2
	s_cbranch_execnz .LBB0_100

.Lattn_k0:
	global_load_dwordx4 v[74:77], v87, s[92:93]
	global_load_dwordx4 v[94:97], v87, s[92:93] offset:64
	global_load_dwordx4 v[120:123], v87, s[92:93] offset:128
	global_load_dwordx4 v[124:127], v87, s[92:93] offset:192
	s_branch .Lattn_skip
